# stream: rotated step order per block on top of rotated wave-row assignment
# baseline (speedup 1.0000x reference)
.LBB1_2:
	s_or_b64 exec, exec, s[0:1]
	s_lshr_b32 s8, s3, 6
	s_add_i32 s8, s8, s2
	s_and_b32 s8, s8, 15
	s_lshl_b32 s0, s2, 7
	v_and_b32_e32 v24, 63, v0
	s_add_i32 s9, s8, s0
	s_waitcnt lgkmcnt(0)
	s_and_b32 s1, s5, 0xffff
	s_mov_b32 s3, 0x20000
	s_brev_b32 s2, 16
	s_mov_b32 s0, s4
	v_lshlrev_b32_e32 v25, 4, v24
	s_lshl_b32 s4, s9, 12
	s_lshr_b32 s11, s9, 7
	s_lshr_b32 s12, s11, 3
	s_add_i32 s11, s11, s12
	s_add_i32 s12, s11, 0
	s_and_b32 s12, s12, 7
	s_lshl_b32 s12, s12, 16
	s_add_i32 s16, s4, s12
	s_add_i32 s12, s11, 1
	s_and_b32 s12, s12, 7
	s_lshl_b32 s12, s12, 16
	s_add_i32 s17, s4, s12
	s_add_i32 s12, s11, 2
	s_and_b32 s12, s12, 7
	s_lshl_b32 s12, s12, 16
	s_add_i32 s18, s4, s12
	s_add_i32 s12, s11, 3
	s_and_b32 s12, s12, 7
	s_lshl_b32 s12, s12, 16
	s_add_i32 s19, s4, s12
	s_add_i32 s12, s11, 4
	s_and_b32 s12, s12, 7
	s_lshl_b32 s12, s12, 16
	s_add_i32 s20, s4, s12
	s_add_i32 s12, s11, 5
	s_and_b32 s12, s12, 7
	s_lshl_b32 s12, s12, 16
	s_add_i32 s21, s4, s12
	s_add_i32 s12, s11, 6
	s_and_b32 s12, s12, 7
	s_lshl_b32 s12, s12, 16
	s_add_i32 s22, s4, s12
	s_add_i32 s12, s11, 7
	s_and_b32 s12, s12, 7
	s_lshl_b32 s12, s12, 16
	s_add_i32 s23, s4, s12
	buffer_load_dwordx4 v[26:29], v25, s[0:3], s16 offen offset:1024 nt
	buffer_load_dwordx4 v[30:33], v25, s[0:3], s16 offen nt
	buffer_load_dwordx4 v[34:37], v25, s[0:3], s16 offen offset:2048 nt
	buffer_load_dwordx4 v[38:41], v25, s[0:3], s17 offen offset:1024 nt
	buffer_load_dwordx4 v[42:45], v25, s[0:3], s17 offen nt
	buffer_load_dwordx4 v[16:19], v25, s[0:3], s16 offen offset:3072 nt
	buffer_load_dwordx4 v[46:49], v25, s[0:3], s17 offen offset:2048 nt
	buffer_load_dwordx4 v[20:23], v25, s[0:3], s17 offen offset:3072 nt
	s_barrier
	buffer_load_dwordx4 v[50:53], v25, s[0:3], s18 offen offset:1024 nt
	buffer_load_dwordx4 v[54:57], v25, s[0:3], s18 offen nt
	ds_read_b128 v[4:7], v25 offset:1024
	ds_read_b128 v[0:3], v25
	ds_read_b128 v[12:15], v25 offset:2048
	ds_read_b128 v[8:11], v25 offset:3072
	v_cmp_gt_u32_e32 vcc, 8, v24
	s_waitcnt vmcnt(9) lgkmcnt(3)
	v_pk_mul_f32 v[28:29], v[6:7], v[28:29]
	v_pk_mul_f32 v[26:27], v[4:5], v[26:27]
	s_waitcnt vmcnt(8) lgkmcnt(2)
	v_pk_fma_f32 v[32:33], v[2:3], v[32:33], v[28:29]
	v_pk_fma_f32 v[30:31], v[0:1], v[30:31], v[26:27]
	buffer_load_dwordx4 v[26:29], v25, s[0:3], s19 offen offset:1024 nt
	s_waitcnt vmcnt(8) lgkmcnt(1)
	v_pk_fma_f32 v[58:59], v[14:15], v[36:37], v[32:33]
	v_pk_fma_f32 v[60:61], v[12:13], v[34:35], v[30:31]
	buffer_load_dwordx4 v[30:33], v25, s[0:3], s19 offen nt
	s_waitcnt vmcnt(8)
	v_pk_mul_f32 v[34:35], v[6:7], v[40:41]
	v_pk_mul_f32 v[36:37], v[4:5], v[38:39]
	s_waitcnt vmcnt(7)
	v_pk_fma_f32 v[44:45], v[2:3], v[44:45], v[34:35]
	v_pk_fma_f32 v[42:43], v[0:1], v[42:43], v[36:37]
	buffer_load_dwordx4 v[34:37], v25, s[0:3], s18 offen offset:2048 nt
	s_waitcnt vmcnt(4)
	v_pk_mul_f32 v[38:39], v[6:7], v[52:53]
	v_pk_mul_f32 v[40:41], v[4:5], v[50:51]
	s_waitcnt vmcnt(3)
	v_pk_fma_f32 v[50:51], v[2:3], v[56:57], v[38:39]
	v_pk_fma_f32 v[52:53], v[0:1], v[54:55], v[40:41]
	buffer_load_dwordx4 v[38:41], v25, s[0:3], s18 offen offset:3072 nt
	v_pk_fma_f32 v[48:49], v[14:15], v[48:49], v[44:45]
	v_pk_fma_f32 v[46:47], v[12:13], v[46:47], v[42:43]
	s_waitcnt lgkmcnt(0)
	v_pk_fma_f32 v[18:19], v[10:11], v[18:19], v[58:59]
	v_pk_fma_f32 v[16:17], v[8:9], v[16:17], v[60:61]
	v_add_f32_e32 v61, v18, v19
	v_add_f32_e32 v60, v16, v17
	v_pk_fma_f32 v[16:17], v[10:11], v[22:23], v[48:49]
	v_pk_fma_f32 v[18:19], v[8:9], v[20:21], v[46:47]
	v_add_f32_e32 v16, v16, v17
	v_add_f32_e32 v18, v18, v19
	v_add_f32_e32 v60, v60, v61
	v_add_f32_e32 v16, v18, v16
	s_waitcnt vmcnt(3)
	v_pk_mul_f32 v[28:29], v[6:7], v[28:29]
	v_pk_mul_f32 v[26:27], v[4:5], v[26:27]
	v_add_f32_dpp v16, v16, v16 quad_perm:[1,0,3,2] row_mask:0xf bank_mask:0xf bound_ctrl:1
	s_waitcnt vmcnt(2)
	v_pk_fma_f32 v[54:55], v[2:3], v[32:33], v[28:29]
	v_pk_fma_f32 v[56:57], v[0:1], v[30:31], v[26:27]
	buffer_load_dwordx4 v[26:29], v25, s[0:3], s19 offen offset:2048 nt
	buffer_load_dwordx4 v[30:33], v25, s[0:3], s19 offen offset:3072 nt
	buffer_load_dwordx4 v[42:45], v25, s[0:3], s20 offen offset:1024 nt
	s_waitcnt vmcnt(4)
	v_pk_fma_f32 v[50:51], v[14:15], v[36:37], v[50:51]
	v_pk_fma_f32 v[52:53], v[12:13], v[34:35], v[52:53]
	buffer_load_dwordx4 v[34:37], v25, s[0:3], s20 offen nt
	v_add_f32_dpp v16, v16, v16 quad_perm:[2,3,0,1] row_mask:0xf bank_mask:0xf bound_ctrl:1
	s_waitcnt vmcnt(4)
	v_pk_fma_f32 v[58:59], v[10:11], v[40:41], v[50:51]
	v_pk_fma_f32 v[38:39], v[8:9], v[38:39], v[52:53]
	v_add_f32_e32 v19, v58, v59
	v_add_f32_e32 v17, v38, v39
	v_add_f32_dpp v58, v60, v60 quad_perm:[1,0,3,2] row_mask:0xf bank_mask:0xf bound_ctrl:1
	v_add_f32_e32 v18, v17, v19
	v_add_f32_dpp v16, v16, v16 row_ror:4 row_mask:0xf bank_mask:0xf bound_ctrl:1
	v_add_f32_dpp v17, v58, v58 quad_perm:[2,3,0,1] row_mask:0xf bank_mask:0xf bound_ctrl:1
	buffer_load_dwordx4 v[20:23], v25, s[0:3], s20 offen offset:2048 nt
	buffer_load_dwordx4 v[46:49], v25, s[0:3], s20 offen offset:3072 nt
	v_add_f32_dpp v17, v17, v17 row_ror:4 row_mask:0xf bank_mask:0xf bound_ctrl:1
	v_add_f32_dpp v58, v16, v16 row_ror:8 row_mask:0xf bank_mask:0xf bound_ctrl:1
	buffer_load_dwordx4 v[38:41], v25, s[0:3], s21 offen nt
	buffer_load_dwordx4 v[50:53], v25, s[0:3], s21 offen offset:1024 nt
	v_add_f32_dpp v17, v17, v17 row_ror:8 row_mask:0xf bank_mask:0xf bound_ctrl:1
	v_mov_b32_e32 v19, v17
	v_mov_b32_e32 v59, v58
	s_nop 0
	v_permlane16_swap_b32_e32 v17, v19
	v_permlane16_swap_b32_e32 v58, v59
	v_add_f32_e32 v16, v17, v19
	v_add_f32_e32 v17, v58, v59
	v_add_f32_dpp v18, v18, v18 quad_perm:[1,0,3,2] row_mask:0xf bank_mask:0xf bound_ctrl:1
	s_waitcnt vmcnt(7)
	v_pk_fma_f32 v[28:29], v[14:15], v[28:29], v[54:55]
	v_pk_fma_f32 v[54:55], v[12:13], v[26:27], v[56:57]
	s_waitcnt vmcnt(6)
	v_pk_fma_f32 v[58:59], v[10:11], v[32:33], v[28:29]
	buffer_load_dwordx4 v[26:29], v25, s[0:3], s21 offen offset:2048 nt
	v_pk_fma_f32 v[54:55], v[8:9], v[30:31], v[54:55]
	buffer_load_dwordx4 v[30:33], v25, s[0:3], s21 offen offset:3072 nt
	v_add_f32_e32 v66, v54, v55
	s_waitcnt vmcnt(7)
	v_pk_mul_f32 v[54:55], v[6:7], v[44:45]
	v_pk_mul_f32 v[56:57], v[4:5], v[42:43]
	buffer_load_dwordx4 v[42:45], v25, s[0:3], s22 offen offset:1024 nt
	s_waitcnt vmcnt(7)
	v_pk_fma_f32 v[54:55], v[2:3], v[36:37], v[54:55]
	v_pk_fma_f32 v[56:57], v[0:1], v[34:35], v[56:57]
	buffer_load_dwordx4 v[34:37], v25, s[0:3], s22 offen nt
	v_add_f32_dpp v18, v18, v18 quad_perm:[2,3,0,1] row_mask:0xf bank_mask:0xf bound_ctrl:1
	s_waitcnt vmcnt(7)
	v_pk_fma_f32 v[22:23], v[14:15], v[22:23], v[54:55]
	v_pk_fma_f32 v[20:21], v[12:13], v[20:21], v[56:57]
	s_waitcnt vmcnt(6)
	v_pk_fma_f32 v[60:61], v[10:11], v[48:49], v[22:23]
	v_pk_fma_f32 v[22:23], v[8:9], v[46:47], v[20:21]
	s_waitcnt vmcnt(4)
	v_pk_mul_f32 v[54:55], v[4:5], v[50:51]
	v_pk_mul_f32 v[20:21], v[6:7], v[52:53]
	v_pk_fma_f32 v[38:39], v[0:1], v[38:39], v[54:55]
	buffer_load_dwordx4 v[46:49], v25, s[0:3], s22 offen offset:2048 nt
	buffer_load_dwordx4 v[50:53], v25, s[0:3], s22 offen offset:3072 nt
	v_pk_fma_f32 v[20:21], v[2:3], v[40:41], v[20:21]
	v_add_f32_e32 v23, v22, v23
	v_add_f32_dpp v18, v18, v18 row_ror:4 row_mask:0xf bank_mask:0xf bound_ctrl:1
	s_waitcnt vmcnt(5)
	v_pk_fma_f32 v[26:27], v[12:13], v[26:27], v[38:39]
	buffer_load_dwordx4 v[38:41], v25, s[0:3], s23 offen nt
	buffer_load_dwordx4 v[54:57], v25, s[0:3], s23 offen offset:1024 nt
	v_pk_fma_f32 v[20:21], v[14:15], v[28:29], v[20:21]
	s_waitcnt vmcnt(6)
	v_pk_fma_f32 v[30:31], v[8:9], v[30:31], v[26:27]
	v_pk_fma_f32 v[62:63], v[10:11], v[32:33], v[20:21]
	v_add_f32_dpp v18, v18, v18 row_ror:8 row_mask:0xf bank_mask:0xf bound_ctrl:1
	s_waitcnt vmcnt(5)
	v_pk_mul_f32 v[20:21], v[6:7], v[44:45]
	v_pk_mul_f32 v[26:27], v[4:5], v[42:43]
	buffer_load_dwordx4 v[42:45], v25, s[0:3], s23 offen offset:2048 nt
	s_waitcnt vmcnt(5)
	v_pk_fma_f32 v[64:65], v[0:1], v[34:35], v[26:27]
	buffer_load_dwordx4 v[32:35], v25, s[0:3], s23 offen offset:3072 nt
	v_add_f32_e32 v27, v60, v61
	v_add_f32_e32 v23, v23, v27
	v_pk_fma_f32 v[36:37], v[2:3], v[36:37], v[20:21]
	v_add_f32_e32 v20, v58, v59
	v_add_f32_dpp v23, v23, v23 quad_perm:[1,0,3,2] row_mask:0xf bank_mask:0xf bound_ctrl:1
	v_add_f32_e32 v20, v66, v20
	v_mov_b32_e32 v19, v18
	v_add_f32_dpp v23, v23, v23 quad_perm:[2,3,0,1] row_mask:0xf bank_mask:0xf bound_ctrl:1
	v_add_f32_dpp v20, v20, v20 quad_perm:[1,0,3,2] row_mask:0xf bank_mask:0xf bound_ctrl:1
	v_permlane16_swap_b32_e32 v18, v19
	v_add_f32_dpp v23, v23, v23 row_ror:4 row_mask:0xf bank_mask:0xf bound_ctrl:1
	v_add_f32_dpp v20, v20, v20 quad_perm:[2,3,0,1] row_mask:0xf bank_mask:0xf bound_ctrl:1
	v_add_f32_e32 v18, v18, v19
	v_add_f32_dpp v23, v23, v23 row_ror:8 row_mask:0xf bank_mask:0xf bound_ctrl:1
	v_mov_b32_e32 v27, v23
	s_nop 1
	v_permlane16_swap_b32_e32 v23, v27
	v_add_f32_e32 v28, v23, v27
	v_add_f32_e32 v23, v30, v31
	s_waitcnt vmcnt(5)
	v_pk_fma_f32 v[30:31], v[14:15], v[48:49], v[36:37]
	v_pk_fma_f32 v[36:37], v[12:13], v[46:47], v[64:65]
	s_waitcnt vmcnt(4)
	v_pk_fma_f32 v[30:31], v[10:11], v[52:53], v[30:31]
	v_pk_fma_f32 v[36:37], v[8:9], v[50:51], v[36:37]
	v_add_f32_e32 v27, v62, v63
	v_add_f32_e32 v36, v36, v37
	v_add_f32_e32 v30, v30, v31
	v_add_f32_e32 v23, v23, v27
	v_add_f32_e32 v30, v36, v30
	v_add_f32_dpp v20, v20, v20 row_ror:4 row_mask:0xf bank_mask:0xf bound_ctrl:1
	v_add_f32_dpp v23, v23, v23 quad_perm:[1,0,3,2] row_mask:0xf bank_mask:0xf bound_ctrl:1
	v_add_f32_dpp v30, v30, v30 quad_perm:[1,0,3,2] row_mask:0xf bank_mask:0xf bound_ctrl:1
	v_add_f32_dpp v20, v20, v20 row_ror:8 row_mask:0xf bank_mask:0xf bound_ctrl:1
	v_add_f32_dpp v23, v23, v23 quad_perm:[2,3,0,1] row_mask:0xf bank_mask:0xf bound_ctrl:1
	v_add_f32_dpp v30, v30, v30 quad_perm:[2,3,0,1] row_mask:0xf bank_mask:0xf bound_ctrl:1
	v_mov_b32_e32 v21, v20
	v_add_f32_dpp v23, v23, v23 row_ror:4 row_mask:0xf bank_mask:0xf bound_ctrl:1
	v_add_f32_dpp v30, v30, v30 row_ror:4 row_mask:0xf bank_mask:0xf bound_ctrl:1
	v_permlane16_swap_b32_e32 v20, v21
	v_add_f32_dpp v23, v23, v23 row_ror:8 row_mask:0xf bank_mask:0xf bound_ctrl:1
	v_add_f32_dpp v30, v30, v30 row_ror:8 row_mask:0xf bank_mask:0xf bound_ctrl:1
	v_mov_b32_e32 v27, v23
	v_mov_b32_e32 v31, v30
	s_nop 0
	v_permlane16_swap_b32_e32 v23, v27
	v_permlane16_swap_b32_e32 v30, v31
	v_add_f32_e32 v21, v20, v21
	v_add_f32_e32 v23, v23, v27
	v_add_f32_e32 v30, v30, v31
	v_mov_b32_e32 v19, v16
	v_mov_b32_e32 v20, v17
	v_mov_b32_e32 v22, v18
	v_mov_b32_e32 v26, v21
	v_mov_b32_e32 v29, v28
	v_mov_b32_e32 v27, v23
	v_mov_b32_e32 v31, v30
	v_permlane32_swap_b32_e32 v16, v19
	v_permlane32_swap_b32_e32 v17, v20
	v_permlane32_swap_b32_e32 v18, v22
	v_permlane32_swap_b32_e32 v21, v26
	v_permlane32_swap_b32_e32 v28, v29
	v_permlane32_swap_b32_e32 v23, v27
	s_waitcnt vmcnt(2)
	v_pk_mul_f32 v[6:7], v[6:7], v[56:57]
	v_pk_mul_f32 v[4:5], v[4:5], v[54:55]
	v_pk_fma_f32 v[2:3], v[2:3], v[40:41], v[6:7]
	v_pk_fma_f32 v[0:1], v[0:1], v[38:39], v[4:5]
	v_permlane32_swap_b32_e32 v30, v31
	s_waitcnt vmcnt(1)
	v_pk_fma_f32 v[2:3], v[14:15], v[44:45], v[2:3]
	v_pk_fma_f32 v[0:1], v[12:13], v[42:43], v[0:1]
	s_waitcnt vmcnt(0)
	v_pk_fma_f32 v[2:3], v[10:11], v[34:35], v[2:3]
	v_pk_fma_f32 v[0:1], v[8:9], v[32:33], v[0:1]
	s_nop 0
	v_add_f32_e32 v0, v0, v1
	v_add_f32_e32 v1, v2, v3
	v_add_f32_e32 v0, v0, v1
	s_nop 1
	v_add_f32_dpp v0, v0, v0 quad_perm:[1,0,3,2] row_mask:0xf bank_mask:0xf bound_ctrl:1
	s_nop 1
	v_add_f32_dpp v0, v0, v0 quad_perm:[2,3,0,1] row_mask:0xf bank_mask:0xf bound_ctrl:1
	s_nop 1
	v_add_f32_dpp v0, v0, v0 row_ror:4 row_mask:0xf bank_mask:0xf bound_ctrl:1
	s_nop 1
	v_add_f32_dpp v0, v0, v0 row_ror:8 row_mask:0xf bank_mask:0xf bound_ctrl:1
	v_mov_b32_e32 v1, v0
	s_nop 1
	v_permlane16_swap_b32_e32 v0, v1
	v_add_f32_e32 v0, v0, v1
	v_mov_b32_e32 v1, v0
	s_nop 1
	v_permlane32_swap_b32_e32 v0, v1
	s_and_saveexec_b64 s[0:1], vcc
	s_cbranch_execz .LBB1_4
	v_add_f32_e32 v6, v16, v19
	v_cmp_eq_u32_e32 vcc, 0, v24
	v_add_f32_e32 v5, v17, v20
	v_add_f32_e32 v4, v18, v22
	v_cndmask_b32_e32 v6, 0, v6, vcc
	v_cmp_eq_u32_e32 vcc, 1, v24
	v_add_f32_e32 v3, v21, v26
	v_add_f32_e32 v2, v28, v29
	v_cndmask_b32_e32 v5, v6, v5, vcc
	v_cmp_eq_u32_e32 vcc, 2, v24
	v_add_f32_e32 v0, v0, v1
	v_add_f32_e32 v1, v30, v31
	v_cndmask_b32_e32 v4, v5, v4, vcc
	v_cmp_eq_u32_e32 vcc, 3, v24
	s_lshl_b32 s0, s8, 13
	s_and_b32 s0, s0, 0x1e000
	v_cndmask_b32_e32 v3, v4, v3, vcc
	v_cmp_eq_u32_e32 vcc, 4, v24
	s_add_u32 s0, s6, s0
	s_addc_u32 s1, s7, 0
	v_cndmask_b32_e32 v2, v3, v2, vcc
	v_add_f32_e32 v3, v23, v27
	v_cmp_eq_u32_e32 vcc, 5, v24
	s_nop 1
	v_cndmask_b32_e32 v2, v2, v3, vcc
	v_cmp_eq_u32_e32 vcc, 6, v24
	s_nop 1
	v_cndmask_b32_e32 v1, v2, v1, vcc
	v_cmp_eq_u32_e32 vcc, 7, v24
	s_nop 1
	v_cndmask_b32_e32 v2, v1, v0, vcc
	v_add_u32_e32 v0, s11, v24
	v_and_b32_e32 v0, 7, v0
	s_lshr_b32 s9, s9, 4
	v_add_u32_e32 v0, s9, v0
	v_ashrrev_i32_e32 v1, 31, v0
	v_lshl_add_u64 v[0:1], v[0:1], 2, s[0:1]
	v_add_co_u32_e32 v0, vcc, 0x6000, v0
	s_nop 1
	v_addc_co_u32_e32 v1, vcc, 0, v1, vcc
	global_store_dword v[0:1], v2, off offset:64

	.amdhsa_kernel _Z13stream_kernelPKfPf
		.amdhsa_group_segment_fixed_size 4096
		.amdhsa_private_segment_fixed_size 0
		.amdhsa_kernarg_size 16
		.amdhsa_user_sgpr_count 2
		.amdhsa_user_sgpr_dispatch_ptr 0
		.amdhsa_user_sgpr_queue_ptr 0
		.amdhsa_user_sgpr_kernarg_segment_ptr 1
		.amdhsa_user_sgpr_dispatch_id 0
		.amdhsa_user_sgpr_kernarg_preload_length 0
		.amdhsa_user_sgpr_kernarg_preload_offset 0
		.amdhsa_user_sgpr_private_segment_size 0
		.amdhsa_uses_dynamic_stack 0
		.amdhsa_enable_private_segment 0
		.amdhsa_system_sgpr_workgroup_id_x 1
		.amdhsa_system_sgpr_workgroup_id_y 0
		.amdhsa_system_sgpr_workgroup_id_z 0
		.amdhsa_system_sgpr_workgroup_info 0
		.amdhsa_system_vgpr_workitem_id 0
		.amdhsa_next_free_vgpr 67
		.amdhsa_next_free_sgpr 24
		.amdhsa_accum_offset 68
		.amdhsa_reserve_vcc 1
		.amdhsa_float_round_mode_32 0
		.amdhsa_float_round_mode_16_64 0
		.amdhsa_float_denorm_mode_32 3
		.amdhsa_float_denorm_mode_16_64 3
		.amdhsa_dx10_clamp 1
		.amdhsa_ieee_mode 1
		.amdhsa_fp16_overflow 0
		.amdhsa_tg_split 0
		.amdhsa_exception_fp_ieee_invalid_op 0
		.amdhsa_exception_fp_denorm_src 0
		.amdhsa_exception_fp_ieee_div_zero 0
		.amdhsa_exception_fp_ieee_overflow 0
		.amdhsa_exception_fp_ieee_underflow 0
		.amdhsa_exception_fp_ieee_inexact 0
		.amdhsa_exception_int_div_zero 0
	.end_amdhsa_kernel

.Lfunc_end1:
	.size	_Z13stream_kernelPKfPf, .Lfunc_end1-_Z13stream_kernelPKfPf
	.set _Z13stream_kernelPKfPf.num_vgpr, 67
	.set _Z13stream_kernelPKfPf.num_agpr, 0
	.set _Z13stream_kernelPKfPf.numbered_sgpr, 24
	.set _Z13stream_kernelPKfPf.num_named_barrier, 0
	.set _Z13stream_kernelPKfPf.private_seg_size, 0
	.set _Z13stream_kernelPKfPf.uses_vcc, 1
	.set _Z13stream_kernelPKfPf.uses_flat_scratch, 0
	.set _Z13stream_kernelPKfPf.has_dyn_sized_stack, 0
	.set _Z13stream_kernelPKfPf.has_recursion, 0
	.set _Z13stream_kernelPKfPf.has_indirect_call, 0

amdhsa.kernels:
  - .agpr_count:     0
    .args:
      - .actual_access:  read_only
        .address_space:  global
        .offset:         0
        .size:           8
        .value_kind:     global_buffer
      - .actual_access:  read_only
        .address_space:  global
        .offset:         8
        .size:           8
        .value_kind:     global_buffer
      - .actual_access:  read_only
        .address_space:  global
        .offset:         16
        .size:           8
        .value_kind:     global_buffer
      - .actual_access:  read_only
        .address_space:  global
        .offset:         24
        .size:           8
        .value_kind:     global_buffer
      - .actual_access:  write_only
        .address_space:  global
        .offset:         32
        .size:           8
        .value_kind:     global_buffer
    .group_segment_fixed_size: 2112
    .kernarg_segment_align: 8
    .kernarg_segment_size: 40
    .language:       OpenCL C
    .language_version:
      - 2
      - 0
    .max_flat_workgroup_size: 1024
    .name:           _Z11prep_kernelPKfS0_S0_S0_Pf
    .private_segment_fixed_size: 0
    .sgpr_count:     32
    .sgpr_spill_count: 0
    .symbol:         _Z11prep_kernelPKfS0_S0_S0_Pf.kd
    .uniform_work_group_size: 1
    .uses_dynamic_stack: false
    .vgpr_count:     40
    .vgpr_spill_count: 0
    .wavefront_size: 64
  - .agpr_count:     0
    .args:
      - .actual_access:  read_only
        .address_space:  global
        .offset:         0
        .size:           8
        .value_kind:     global_buffer
      - .address_space:  global
        .offset:         8
        .size:           8
        .value_kind:     global_buffer
    .group_segment_fixed_size: 4096
    .kernarg_segment_align: 8
    .kernarg_segment_size: 16
    .language:       OpenCL C
    .language_version:
      - 2
      - 0
    .max_flat_workgroup_size: 1024
    .name:           _Z13stream_kernelPKfPf
    .private_segment_fixed_size: 0
    .sgpr_count:     30
    .sgpr_spill_count: 0
    .symbol:         _Z13stream_kernelPKfPf.kd
    .uniform_work_group_size: 1
    .uses_dynamic_stack: false
    .vgpr_count:     67
    .vgpr_spill_count: 0
    .wavefront_size: 64
  - .agpr_count:     0
    .args:
      - .actual_access:  read_only
        .address_space:  global
        .offset:         0
        .size:           8
        .value_kind:     global_buffer
      - .actual_access:  write_only
        .address_space:  global
        .offset:         8
        .size:           8
        .value_kind:     global_buffer
    .group_segment_fixed_size: 32
    .kernarg_segment_align: 8
    .kernarg_segment_size: 16
    .language:       OpenCL C
    .language_version:
      - 2
      - 0
    .max_flat_workgroup_size: 256
    .name:           _Z14softmax_kernelPKfPf
    .private_segment_fixed_size: 0
    .sgpr_count:     16
    .sgpr_spill_count: 0
    .symbol:         _Z14softmax_kernelPKfPf.kd
    .uniform_work_group_size: 1
    .uses_dynamic_stack: false
    .vgpr_count:     17
    .vgpr_spill_count: 0
    .wavefront_size: 64
